# v47 + bf16 weight tiles 1472..4095 (w_out, dense FFN) converted by a hand-written 2-slot pipelined routine at the in-proj layer-0 hook entry; P0a converts pairs < 736 only
# speedup vs baseline: 1.0074x; 1.0074x over previous
; #define CV_LOAD(j, R) do { ConvTile c_; if (CV_VALID(j) && CV_DEC(CV_TILE(j), c_)) conv_load(c_.W, c_.N, c_.k0, c_.n0, wave, lane, R); } while (0)
; template <int NSLOT, bool MOE> __device__ __forceinline__ void conv_burst(const ConvHook& h, int bid, PG8_LAS unsigned char* T_, int tid) {
;     ...
;     const int p0 = (h.t0 >> 1) + bid, p1 = h.t1 >> 1;
;     ...
;     if constexpr (NSLOT == 4) {
;         f32x4 R0[8], R1[8], R2[8], R3[8];
;         CV_LOAD(0, R0); CV_LOAD(1, R1); CV_LOAD(2, R2);
.LBB0_73:
	s_or_b64 exec, exec, s[10:11]
	v_readfirstlane_b32 s4, v82
	s_ashr_i32 s12, s4, 6
	s_mov_b64 s[10:11], s[92:93]
	s_cmpk_gt_i32 s3, 0x2df
	s_waitcnt lgkmcnt(0)
	s_barrier
	s_cbranch_scc1 .LBB0_78
	s_lshl_b32 s13, s3, 1
	s_cmpk_gt_i32 s3, 0x2df
	s_cbranch_scc0 .LBB0_79
	s_cmpk_gt_u32 s13, 0x7bf
	s_cbranch_scc0 .LBB0_80
	s_cmpk_gt_u32 s13, 0xd3f
	s_cbranch_scc0 .LBB0_81
	s_load_dwordx2 s[8:9], s[10:11], 0xc0
	s_lshl_b32 s4, s3, 4
	s_add_i32 s4, s4, 0x7fff9600
	s_and_b32 s7, s4, 0x7fffffc0
	s_and_b32 s15, s14, 0x600
	s_mov_b64 s[4:5], 0
	s_branch .LBB0_82

; #define CV_LOAD(j, R) do { ConvTile c_; if (CV_VALID(j) && CV_DEC(CV_TILE(j), c_)) conv_load(c_.W, c_.N, c_.k0, c_.n0, wave, lane, R); } while (0)
; template <int NSLOT, bool MOE> __device__ __forceinline__ void conv_burst(const ConvHook& h, int bid, PG8_LAS unsigned char* T_, int tid) {
;     ...
;     if constexpr (NSLOT == 4) {
;         f32x4 R0[8], R1[8], R2[8], R3[8];
;         CV_LOAD(0, R0); CV_LOAD(1, R1); CV_LOAD(2, R2);
.LBB0_123:
	s_mov_b64 s[4:5], -1
	s_cmpk_lt_i32 s3, 0x1e0
	v_readfirstlane_b32 s33, v0
	s_cbranch_scc1 .LBB0_125
	v_lshlrev_b32_e32 v66, 2, v83
	s_lshl_b32 s33, s12, 3
	s_mov_b64 s[4:5], 0

; #define CV_LOAD(j, R) do { ConvTile c_; if (CV_VALID(j) && CV_DEC(CV_TILE(j), c_)) conv_load(c_.W, c_.N, c_.k0, c_.n0, wave, lane, R); } while (0)
; #define CV_PROC(j, R) { ConvTile c_; if (!CV_VALID(j) || !CV_DEC(CV_TILE(j), c_)) break; if constexpr (MOE) conv_emit_moe(c_, R, T, tid, wave, lane); else conv_emit(c_, R, T, tid, wave, lane); }
; template <int NSLOT, bool MOE> __device__ __forceinline__ void conv_burst(const ConvHook& h, int bid, PG8_LAS unsigned char* T_, int tid) {
;     ...
;     if constexpr (NSLOT == 4) {
;         f32x4 R0[8], R1[8], R2[8], R3[8];
;         CV_LOAD(0, R0); CV_LOAD(1, R1); CV_LOAD(2, R2);
;         for (int j = 0;; j += 4) {
;             CV_LOAD(j + 3, R3); CV_PROC(j, R0)
;             CV_LOAD(j + 4, R0); CV_PROC(j + 1, R1)
;             CV_LOAD(j + 5, R1); CV_PROC(j + 2, R2)
;             CV_LOAD(j + 6, R2); CV_PROC(j + 3, R3)
;         }
.LBB0_153:
	s_and_b32 s8, s45, 0x7ffffe00
	s_add_i32 s58, s3, s8
	s_addk_i32 s58, 0x100
	s_cmpk_lt_i32 s58, 0x2e0
	s_cselect_b64 s[14:15], -1, 0
	s_cmpk_gt_i32 s58, 0x2df
	s_cbranch_scc1 .LBB0_177
	s_lshl_b32 s12, s58, 1
	s_or_b32 s27, s12, 1
	s_cmpk_lt_i32 s27, 0x6400
	s_cselect_b64 s[8:9], -1, 0
	s_cmpk_gt_i32 s27, 0x63ff
	s_cbranch_scc1 .LBB0_167
	s_cmpk_gt_i32 s27, 0x5bf
	s_waitcnt lgkmcnt(0)
	s_mov_b64 s[28:29], -1
	s_cbranch_scc0 .LBB0_165
	s_cmpk_gt_u32 s12, 0x7bf
	s_cbranch_scc0 .LBB0_162
	s_cmpk_gt_u32 s12, 0xd3f
	s_mov_b64 s[24:25], -1
	s_cbranch_scc0 .LBB0_159
	s_load_dwordx2 s[18:19], s[10:11], 0xc0
	s_lshl_b32 s24, s58, 4
	s_add_i32 s24, s24, 0x7fff9600
	s_and_b32 s46, s24, 0x7fffffc0
	s_lshl_b32 s24, s27, 8
	s_and_b32 s50, s24, 0x700
	s_mov_b64 s[24:25], 0

; #define CV_LOAD(j, R) do { ConvTile c_; if (CV_VALID(j) && CV_DEC(CV_TILE(j), c_)) conv_load(c_.W, c_.N, c_.k0, c_.n0, wave, lane, R); } while (0)
; #define CV_PROC(j, R) { ConvTile c_; if (!CV_VALID(j) || !CV_DEC(CV_TILE(j), c_)) break; if constexpr (MOE) conv_emit_moe(c_, R, T, tid, wave, lane); else conv_emit(c_, R, T, tid, wave, lane); }
; template <int NSLOT, bool MOE> __device__ __forceinline__ void conv_burst(const ConvHook& h, int bid, PG8_LAS unsigned char* T_, int tid) {
;     ...
;     if constexpr (NSLOT == 4) {
;         f32x4 R0[8], R1[8], R2[8], R3[8];
;         CV_LOAD(0, R0); CV_LOAD(1, R1); CV_LOAD(2, R2);
;         for (int j = 0;; j += 4) {
;             CV_LOAD(j + 3, R3); CV_PROC(j, R0)
;             CV_LOAD(j + 4, R0); CV_PROC(j + 1, R1)
;             CV_LOAD(j + 5, R1); CV_PROC(j + 2, R2)
;             CV_LOAD(j + 6, R2); CV_PROC(j + 3, R3)
;         }
.LBB0_177:
	s_add_i32 s25, s3, s45
	s_cmpk_gt_i32 s25, 0x2df
	s_mov_b64 s[8:9], -1
	s_cbranch_scc1 .LBB0_152
	s_waitcnt lgkmcnt(0)
	s_load_dwordx2 s[28:29], s[10:11], 0xf8
	s_add_i32 s27, s40, 0xffff0480
	s_cmpk_gt_i32 s25, 0x2df
	s_cbranch_scc0 .LBB0_217
	s_cmpk_gt_u32 s27, 0x7bf
	s_cbranch_scc0 .LBB0_184
	s_cmpk_gt_u32 s27, 0xd3f
	s_cbranch_scc0 .LBB0_182
	s_waitcnt lgkmcnt(0)
	s_add_u32 s34, s28, 0x7a00000
	s_addc_u32 s35, s29, 0
	s_add_i32 s8, s39, 0xffffd000
	s_and_b32 s36, s8, 0x7fffffc0
	s_add_i32 s8, s38, 0xfffc0000
	s_and_b32 s12, s8, 0x600
	s_mov_b64 s[8:9], 0

; #define CV_LOAD(j, R) do { ConvTile c_; if (CV_VALID(j) && CV_DEC(CV_TILE(j), c_)) conv_load(c_.W, c_.N, c_.k0, c_.n0, wave, lane, R); } while (0)
; #define CV_PROC(j, R) { ConvTile c_; if (!CV_VALID(j) || !CV_DEC(CV_TILE(j), c_)) break; if constexpr (MOE) conv_emit_moe(c_, R, T, tid, wave, lane); else conv_emit(c_, R, T, tid, wave, lane); }
; template <int NSLOT, bool MOE> __device__ __forceinline__ void conv_burst(const ConvHook& h, int bid, PG8_LAS unsigned char* T_, int tid) {
;     ...
;     if constexpr (NSLOT == 4) {
;         f32x4 R0[8], R1[8], R2[8], R3[8];
;         CV_LOAD(0, R0); CV_LOAD(1, R1); CV_LOAD(2, R2);
;         for (int j = 0;; j += 4) {
;             CV_LOAD(j + 3, R3); CV_PROC(j, R0)
;             CV_LOAD(j + 4, R0); CV_PROC(j + 1, R1)
;             CV_LOAD(j + 5, R1); CV_PROC(j + 2, R2)
;             CV_LOAD(j + 6, R2); CV_PROC(j + 3, R3)
;         }
.LBB0_233:
	s_add_i32 s36, s25, 0x200
	s_cmpk_lt_i32 s36, 0x2e0
	s_cselect_b64 s[30:31], -1, 0
	s_cmpk_gt_i32 s36, 0x2df
	s_cbranch_scc1 .LBB0_257
	s_add_i32 s37, s40, 0xffff0880
	s_cmpk_gt_i32 s36, 0x2df
	s_mov_b64 s[34:35], -1
	s_cbranch_scc0 .LBB0_244
	s_cmpk_gt_u32 s37, 0x7bf
	s_cbranch_scc0 .LBB0_241
	s_cmpk_gt_u32 s37, 0xd3f
	s_cbranch_scc0 .LBB0_238
	s_load_dwordx2 s[8:9], s[10:11], 0xc0
	s_add_i32 s12, s39, 0xfffff000
	s_and_b32 s59, s12, 0x7fffffc0
	s_and_b32 s60, s38, 0x600
	s_mov_b64 s[34:35], 0

; #define CV_LOAD(j, R) do { ConvTile c_; if (CV_VALID(j) && CV_DEC(CV_TILE(j), c_)) conv_load(c_.W, c_.N, c_.k0, c_.n0, wave, lane, R); } while (0)
; #define CV_PROC(j, R) { ConvTile c_; if (!CV_VALID(j) || !CV_DEC(CV_TILE(j), c_)) break; if constexpr (MOE) conv_emit_moe(c_, R, T, tid, wave, lane); else conv_emit(c_, R, T, tid, wave, lane); }
; template <int NSLOT, bool MOE> __device__ __forceinline__ void conv_burst(const ConvHook& h, int bid, PG8_LAS unsigned char* T_, int tid) {
;     ...
;     if constexpr (NSLOT == 4) {
;         f32x4 R0[8], R1[8], R2[8], R3[8];
;         CV_LOAD(0, R0); CV_LOAD(1, R1); CV_LOAD(2, R2);
;         for (int j = 0;; j += 4) {
;             CV_LOAD(j + 3, R3); CV_PROC(j, R0)
;             CV_LOAD(j + 4, R0); CV_PROC(j + 1, R1)
;             CV_LOAD(j + 5, R1); CV_PROC(j + 2, R2)
;             CV_LOAD(j + 6, R2); CV_PROC(j + 3, R3)
;         }
.LBB0_340:
	s_add_i32 s27, s25, 0x100
	s_cmpk_gt_i32 s27, 0x2df
	s_mov_b64 s[8:9], -1
	s_cbranch_scc1 .LBB0_152
	s_add_i32 s37, s40, 0xffff0680
	s_cmpk_gt_i32 s27, 0x2df
	s_cbranch_scc0 .LBB0_402
	s_cmpk_gt_u32 s37, 0x7bf
	s_cbranch_scc0 .LBB0_347
	s_cmpk_gt_u32 s37, 0xd3f
	s_cbranch_scc0 .LBB0_345
	s_waitcnt lgkmcnt(0)
	s_add_u32 s34, s28, 0x7a00000
	s_addc_u32 s35, s29, 0
	s_add_i32 s8, s39, 0xffffe000
	s_and_b32 s59, s8, 0x7fffffc0
	s_add_i32 s8, s38, 0xfffe0000
	s_and_b32 s12, s8, 0x600
	s_mov_b64 s[8:9], 0

; #define CV_LOAD(j, R) do { ConvTile c_; if (CV_VALID(j) && CV_DEC(CV_TILE(j), c_)) conv_load(c_.W, c_.N, c_.k0, c_.n0, wave, lane, R); } while (0)
; #define CV_PROC(j, R) { ConvTile c_; if (!CV_VALID(j) || !CV_DEC(CV_TILE(j), c_)) break; if constexpr (MOE) conv_emit_moe(c_, R, T, tid, wave, lane); else conv_emit(c_, R, T, tid, wave, lane); }
; template <int NSLOT, bool MOE> __device__ __forceinline__ void conv_burst(const ConvHook& h, int bid, PG8_LAS unsigned char* T_, int tid) {
;     ...
;         for (int j = 0;; j += 4) {
;             CV_LOAD(j + 3, R3); CV_PROC(j, R0)
;             CV_LOAD(j + 4, R0); CV_PROC(j + 1, R1)
;             CV_LOAD(j + 5, R1); CV_PROC(j + 2, R2)
;             CV_LOAD(j + 6, R2); CV_PROC(j + 3, R3)
;         }
.LBB0_380:
	s_addk_i32 s25, 0x300
	s_cmpk_gt_i32 s25, 0x2df
	s_cbranch_scc1 .LBB0_418

; #define CV_LOAD(j, R) do { ConvTile c_; if (CV_VALID(j) && CV_DEC(CV_TILE(j), c_)) conv_load(c_.W, c_.N, c_.k0, c_.n0, wave, lane, R); } while (0)
; #define CV_PROC(j, R) { ConvTile c_; if (!CV_VALID(j) || !CV_DEC(CV_TILE(j), c_)) break; if constexpr (MOE) conv_emit_moe(c_, R, T, tid, wave, lane); else conv_emit(c_, R, T, tid, wave, lane); }
; template <int NSLOT, bool MOE> __device__ __forceinline__ void conv_burst(const ConvHook& h, int bid, PG8_LAS unsigned char* T_, int tid) {
;     ...
;         for (int j = 0;; j += 4) {
;             CV_LOAD(j + 3, R3); CV_PROC(j, R0)
;             CV_LOAD(j + 4, R0); CV_PROC(j + 1, R1)
;             CV_LOAD(j + 5, R1); CV_PROC(j + 2, R2)
;             CV_LOAD(j + 6, R2); CV_PROC(j + 3, R3)
;         }
.LBB0_417:
	s_or_b64 exec, exec, s[8:9]
	s_waitcnt lgkmcnt(0)
	s_barrier
	s_addk_i32 s25, 0x300
	s_cmpk_gt_i32 s25, 0x2df
	s_cbranch_scc0 .LBB0_381

; __device__ __forceinline__ unsigned cvt_pk_bf16(float lo, float hi) { unsigned r; asm volatile("v_cvt_pk_bf16_f32 %0, %1, %2" : "=v"(r) : "v"(lo), "v"(hi)); return r; }
; #define CV_LOAD(j, R) do { ConvTile c_; if (CV_VALID(j) && CV_DEC(CV_TILE(j), c_)) conv_load(c_.W, c_.N, c_.k0, c_.n0, wave, lane, R); } while (0)
;     __device__ __forceinline__ void operator()(const f32x4 (&acc)[2][2][4][2], const Unit& u, int wr, int wc, int fr, int fq) const {
;         bf16_t* O = (bf16_t*)(ws + WS_P); const int row0 = u.pm * BM + wr * 64 + fr, col0 = u.pn * BM + wc * 32 + 8 * fq;
; #pragma unroll
;         for (int ai = 0; ai < 2; ++ai)
; #pragma unroll
;             for (int m = 0; m < 4; ++m) { bf16_t* rowp = O + (size_t)(row0 + ai * HALF + m * 16) * NP + col0;
; #pragma unroll
;                 for (int bj = 0; bj < 2; ++bj) { const f32x4 v0 = acc[ai][bj][m][0], v1 = acc[ai][bj][m][1];
;                     u32x4 w; w.x = cvt_pk_bf16(v0[0], v0[1]); w.y = cvt_pk_bf16(v0[2], v0[3]); w.z = cvt_pk_bf16(v1[0], v1[1]); w.w = cvt_pk_bf16(v1[2], v1[3]);
;                     *(u32x4*)(rowp + bj * HALF) = w; } }
; template <int NSLOT, bool MOE> __device__ __forceinline__ void conv_burst(const ConvHook& h, int bid, PG8_LAS unsigned char* T_, int tid) {
;     ...
;     if constexpr (NSLOT == 4) {
;         f32x4 R0[8], R1[8], R2[8], R3[8];
;         CV_LOAD(0, R0); CV_LOAD(1, R1); CV_LOAD(2, R2);
.LBB0_760:
	v_lshl_or_b32 v132, s4, 8, v162
	v_ashrrev_i32_e32 v133, 31, v132
	v_lshl_add_u32 v131, s14, 8, v151
	v_lshl_add_u64 v[132:133], v[132:133], 1, s[22:23]
	v_mad_i64_i32 v[148:149], s[4:5], v131, s66, v[132:133]
	v_cvt_pk_bf16_f32 v126, v126, v127
	v_cvt_pk_bf16_f32 v127, v128, v129
	v_cvt_pk_bf16_f32 v128, v122, v123
	v_cvt_pk_bf16_f32 v129, v124, v125
	global_store_dwordx4 v[148:149], v[126:129], off
	v_cvt_pk_bf16_f32 v114, v114, v115
	v_cvt_pk_bf16_f32 v115, v116, v117
	v_cvt_pk_bf16_f32 v116, v106, v107
	v_or_b32_e32 v106, 16, v131
	v_cvt_pk_bf16_f32 v117, v108, v109
	global_store_dwordx4 v[148:149], v[114:117], off offset:256
	v_readlane_b32 s1, v254, 30
	s_cmp_lg_u32 s0, s1
	v_mad_i64_i32 v[114:115], s[4:5], v106, s66, v[132:133]
	v_cvt_pk_bf16_f32 v106, v118, v119
	v_cvt_pk_bf16_f32 v107, v120, v121
	v_cvt_pk_bf16_f32 v108, v110, v111
	v_cvt_pk_bf16_f32 v109, v112, v113
	global_store_dwordx4 v[114:115], v[106:109], off
	v_cvt_pk_bf16_f32 v98, v98, v99
	v_cvt_pk_bf16_f32 v99, v100, v101
	v_cvt_pk_bf16_f32 v100, v90, v91
	v_or_b32_e32 v90, 32, v131
	v_cvt_pk_bf16_f32 v101, v92, v93
	global_store_dwordx4 v[114:115], v[98:101], off offset:256
	s_nop 1
	v_mad_i64_i32 v[98:99], s[4:5], v90, s66, v[132:133]
	v_cvt_pk_bf16_f32 v90, v102, v103
	v_cvt_pk_bf16_f32 v91, v104, v105
	v_cvt_pk_bf16_f32 v92, v94, v95
	v_cvt_pk_bf16_f32 v93, v96, v97
	global_store_dwordx4 v[98:99], v[90:93], off
	v_cvt_pk_bf16_f32 v82, v82, v83
	v_cvt_pk_bf16_f32 v83, v84, v85
	v_cvt_pk_bf16_f32 v84, v74, v75
	v_or_b32_e32 v74, 48, v131
	v_cvt_pk_bf16_f32 v85, v76, v77
	global_store_dwordx4 v[98:99], v[82:85], off offset:256
	s_nop 1
	v_mad_i64_i32 v[82:83], s[4:5], v74, s66, v[132:133]
	v_cvt_pk_bf16_f32 v74, v86, v87
	v_cvt_pk_bf16_f32 v75, v88, v89
	v_cvt_pk_bf16_f32 v76, v78, v79
	v_cvt_pk_bf16_f32 v77, v80, v81
	global_store_dwordx4 v[82:83], v[74:77], off
	v_cvt_pk_bf16_f32 v70, v70, v71
	v_cvt_pk_bf16_f32 v71, v72, v73
	v_cvt_pk_bf16_f32 v72, v66, v67
	v_add_u32_e32 v66, 0x80, v131
	v_mad_i64_i32 v[66:67], s[4:5], v66, s66, v[132:133]
	v_cvt_pk_bf16_f32 v73, v68, v69
	global_store_dwordx4 v[82:83], v[70:73], off offset:256
	v_cvt_pk_bf16_f32 v62, v62, v63
	v_cvt_pk_bf16_f32 v63, v64, v65
	v_cvt_pk_bf16_f32 v64, v58, v59
	v_cvt_pk_bf16_f32 v65, v60, v61
	global_store_dwordx4 v[66:67], v[62:65], off
	v_cvt_pk_bf16_f32 v50, v50, v51
	v_cvt_pk_bf16_f32 v51, v52, v53
	v_cvt_pk_bf16_f32 v52, v42, v43
	v_add_u32_e32 v42, 0x90, v131
	v_cvt_pk_bf16_f32 v53, v44, v45
	global_store_dwordx4 v[66:67], v[50:53], off offset:256
	s_nop 1
	v_mad_i64_i32 v[50:51], s[4:5], v42, s66, v[132:133]
	v_cvt_pk_bf16_f32 v42, v54, v55
	v_cvt_pk_bf16_f32 v43, v56, v57
	v_cvt_pk_bf16_f32 v44, v46, v47
	v_cvt_pk_bf16_f32 v45, v48, v49
	global_store_dwordx4 v[50:51], v[42:45], off
	v_cvt_pk_bf16_f32 v34, v34, v35
	v_cvt_pk_bf16_f32 v35, v36, v37
	v_cvt_pk_bf16_f32 v36, v26, v27
	v_add_u32_e32 v26, 0xa0, v131
	v_cvt_pk_bf16_f32 v37, v28, v29
	global_store_dwordx4 v[50:51], v[34:37], off offset:256
	s_nop 1
	v_mad_i64_i32 v[34:35], s[4:5], v26, s66, v[132:133]
	v_cvt_pk_bf16_f32 v26, v38, v39
	v_cvt_pk_bf16_f32 v27, v40, v41
	v_cvt_pk_bf16_f32 v28, v30, v31
	v_cvt_pk_bf16_f32 v29, v32, v33
	global_store_dwordx4 v[34:35], v[26:29], off
	v_cvt_pk_bf16_f32 v18, v18, v19
	v_cvt_pk_bf16_f32 v19, v20, v21
	v_cvt_pk_bf16_f32 v20, v10, v11
	v_add_u32_e32 v10, 0xb0, v131
	v_cvt_pk_bf16_f32 v21, v12, v13
	global_store_dwordx4 v[34:35], v[18:21], off offset:256
	s_nop 1
	v_mad_i64_i32 v[18:19], s[4:5], v10, s66, v[132:133]
	v_cvt_pk_bf16_f32 v10, v22, v23
	v_cvt_pk_bf16_f32 v11, v24, v25
	v_cvt_pk_bf16_f32 v12, v14, v15
	v_cvt_pk_bf16_f32 v13, v16, v17
	global_store_dwordx4 v[18:19], v[10:13], off
	v_cvt_pk_bf16_f32 v6, v6, v7
	v_cvt_pk_bf16_f32 v7, v8, v9
	v_cvt_pk_bf16_f32 v8, v2, v3
	v_cvt_pk_bf16_f32 v9, v4, v5
	global_store_dwordx4 v[18:19], v[6:9], off offset:256
	s_cbranch_scc1 .LBB0_947
	v_readlane_b32 s4, v254, 34
	v_readfirstlane_b32 s0, v150
	v_mov_b32_e32 v29, 0
	v_readlane_b32 s5, v254, 35
	s_mov_b64 s[14:15], s[92:93]
	s_ashr_i32 s0, s0, 6
	s_andn2_b64 vcc, exec, s[4:5]
	v_mov_b32_e32 v28, v29
	v_mov_b32_e32 v27, v29
	v_mov_b32_e32 v26, v29
	v_mov_b32_e32 v33, v29
	v_mov_b32_e32 v32, v29
	v_mov_b32_e32 v31, v29
	v_mov_b32_e32 v30, v29
	v_mov_b32_e32 v25, v29
	v_mov_b32_e32 v24, v29
	v_mov_b32_e32 v23, v29
	v_mov_b32_e32 v22, v29
	v_mov_b32_e32 v21, v29
	v_mov_b32_e32 v20, v29
	v_mov_b32_e32 v19, v29
	v_mov_b32_e32 v18, v29
	v_mov_b32_e32 v17, v29
	v_mov_b32_e32 v16, v29
	v_mov_b32_e32 v15, v29
	v_mov_b32_e32 v14, v29
	v_mov_b32_e32 v13, v29
	v_mov_b32_e32 v12, v29
	v_mov_b32_e32 v11, v29
	v_mov_b32_e32 v10, v29
	v_mov_b32_e32 v9, v29
	v_mov_b32_e32 v8, v29
	v_mov_b32_e32 v7, v29
	v_mov_b32_e32 v6, v29
	v_mov_b32_e32 v5, v29
	v_mov_b32_e32 v4, v29
	v_mov_b32_e32 v3, v29
	v_mov_b32_e32 v2, v29
	s_cbranch_vccnz .LBB0_787
	v_readlane_b32 s101, v253, 62
	s_nop 3
	s_cmp_eq_u32 s101, 0
	s_cbranch_scc1 .Lhc_skip
; #define GAS __attribute__((address_space(1)))
; __device__ __forceinline__ void conv_load(const float* W, int N, int k0, int n0, int wave, int lane, f32x4 (&r)[8]) {
;     const int n = n0 + 4 * lane; const bool ok = n < N;
;     const float* p = W + (size_t)(k0 + 8 * wave) * N + n;
; #pragma unroll
;     for (int i = 0; i < 8; ++i) r[i] = ok ? __builtin_nontemporal_load((const GAS f32x4*)(p + (size_t)i * N)) : (f32x4){0.f, 0.f, 0.f, 0.f};
; __device__ __forceinline__ bool conv_decode(KA A, int t, ConvTile& c) {
;     unsigned char* ws = A->ws; c.f8 = 0;
;     if (t >= 25600) return false;
;     if (t < 1472) { const int l = t / 736, r = t % 736; c.W = A->in[I_WIN] + (size_t)l * D * PSRC; c.WT = ws + WS_WIN + (size_t)l * NP * D * 2; c.K = D; c.N = PSRC; c.k0 = 64 * (r / 23); c.n0 = 256 * (r % 23); c.kind = 1; return true; } t -= 1472;
;     if (t < 512) { const int l = t >> 8, r = t & 255; c.W = A->in[I_WOUT] + (size_t)l * D * D; c.WT = ws + WS_WOUT + (size_t)l * D * D * 2; c.K = D; c.N = D; c.k0 = 64 * (r >> 3); c.n0 = 256 * (r & 7); c.kind = 0; return true; } t -= 512;
;     if (t < 1408) { const int hf = t / 704, r = t % 704; c.W = hf ? A->in[I_FWU] : A->in[I_FWG]; c.WT = ws + WS_FUP; c.K = D; c.N = FF; c.k0 = 64 * (r / 22); c.n0 = 256 * (r % 22); c.kind = 2 + hf; return true; } t -= 1408;
;     if (t < 704) { c.W = A->in[I_FWD]; c.WT = ws + WS_FDN; c.K = FF; c.N = D; c.k0 = 64 * (t >> 3); c.n0 = 256 * (t & 7); c.kind = 0; return true; } t -= 704;
	v_writelane_b32 v255, s4, 25
	v_writelane_b32 v255, s5, 26
	v_writelane_b32 v255, s6, 27
	v_writelane_b32 v255, s7, 28
	v_writelane_b32 v255, s8, 29
	v_writelane_b32 v255, s9, 30
	v_writelane_b32 v255, s10, 31
	v_writelane_b32 v255, s11, 32
	v_writelane_b32 v255, s12, 33
	v_writelane_b32 v255, s13, 34
	v_writelane_b32 v255, s14, 35
	v_writelane_b32 v255, s15, 36
	v_writelane_b32 v255, s16, 37
	v_writelane_b32 v255, s17, 38
	v_writelane_b32 v255, s18, 39
	v_writelane_b32 v255, s19, 40
	v_writelane_b32 v255, s20, 41
	v_writelane_b32 v255, s21, 42
	v_writelane_b32 v255, s22, 43
	v_writelane_b32 v255, s23, 44
	v_writelane_b32 v255, s24, 45
	v_writelane_b32 v255, s25, 46
	v_writelane_b32 v255, s26, 47
	v_writelane_b32 v255, s27, 48
	v_writelane_b32 v255, s28, 49
	v_writelane_b32 v255, s29, 50
	v_writelane_b32 v255, s30, 51
	v_writelane_b32 v255, s31, 52
	v_writelane_b32 v255, s32, 53
	v_writelane_b32 v255, s33, 54
	v_writelane_b32 v255, s34, 55
	v_writelane_b32 v255, s35, 56
	v_writelane_b32 v255, s36, 57
	v_writelane_b32 v255, s37, 58
	v_writelane_b32 v255, s38, 59
	v_writelane_b32 v255, s39, 60
	v_readlane_b32 s24, v254, 3
	v_readlane_b32 s25, v254, 4
	v_readlane_b32 s29, v254, 2
	s_nop 4
	s_load_dwordx2 s[26:27], s[24:25], 0xf8
	v_readfirstlane_b32 s28, v0
	s_nop 3
	s_lshr_b32 s28, s28, 6
	v_and_b32_e32 v66, 63, v0
	v_and_b32_e32 v67, 7, v0
	v_lshrrev_b32_e32 v68, 3, v0
	v_and_b32_e32 v69, 31, v66
	v_lshlrev_b32_e32 v69, 9, v69
	v_and_b32_e32 v70, 7, v66
	v_xor_b32_e32 v70, s28, v70
	v_lshl_add_u32 v69, v70, 4, v69
	v_add_u32_e32 v69, 0x20000, v69
	v_lshrrev_b32_e32 v70, 2, v68
	v_and_b32_e32 v70, 7, v70
	v_xor_b32_e32 v70, v67, v70
	v_lshlrev_b32_e32 v70, 4, v70
	v_lshl_add_u32 v70, v68, 7, v70
	v_add_u32_e32 v70, 0x20000, v70
	v_lshlrev_b32_e32 v72, 4, v66
	s_add_i32 s15, s29, 0x2e0
	s_waitcnt lgkmcnt(0)
	s_lshl_b32 s14, s15, 1
	s_cmpk_lt_u32 s14, 0x7c0
	s_cbranch_scc0 .Lhc_d1_A1
	s_sub_i32 s17, s14, 0x5c0
	s_lshr_b32 s18, s17, 8
	s_and_b32 s17, s17, 255
	s_load_dwordx2 s[4:5], s[24:25], 0x48
	s_lshl_b32 s19, s18, 24
	s_lshl_b32 s20, s18, 23
	s_add_u32 s6, s26, 0x3e00000
	s_addc_u32 s7, s27, 0
	s_add_u32 s6, s6, s20
	s_addc_u32 s7, s7, 0
	s_movk_i32 s8, 0x800
	s_movk_i32 s9, 0x1000
	s_lshr_b32 s10, s17, 3
	s_lshl_b32 s10, s10, 6
	s_and_b32 s11, s17, 7
	s_lshl_b32 s11, s11, 8
	s_mov_b32 s12, s11
	s_movk_i32 s13, 0x80
	s_waitcnt lgkmcnt(0)
	s_add_u32 s4, s4, s19
	s_addc_u32 s5, s5, 0
	s_branch .Lhc_dd_A1
.Lhc_d1_A1:
	s_cmpk_lt_u32 s14, 0xd40
	s_cbranch_scc0 .Lhc_d2_A1
	s_sub_i32 s17, s14, 0x7c0
	s_cmpk_ge_u32 s17, 0x2c0
	s_cselect_b32 s18, 1, 0
	s_mul_i32 s19, s18, 0x2c0
	s_sub_i32 s17, s17, s19
	s_lshl_b32 s19, s18, 3
	s_add_u32 s20, s24, s19
	s_addc_u32 s21, s25, 0
	s_load_dwordx2 s[4:5], s[20:21], 0xb0
	s_add_u32 s6, s26, 0x4e00000
	s_addc_u32 s7, s27, 0
	s_movk_i32 s8, 0x1600
	s_movk_i32 s9, 0x1000
	s_mul_i32 s19, s17, 0xba3
	s_lshr_b32 s19, s19, 16
	s_lshl_b32 s10, s19, 6
	s_mul_i32 s19, s19, 22
	s_sub_i32 s19, s17, s19
	s_lshl_b32 s11, s19, 8
	s_lshl_b32 s12, s11, 1
	s_lshl_b32 s19, s18, 7
	s_add_i32 s12, s12, s19
	s_movk_i32 s13, 0x100
	s_waitcnt lgkmcnt(0)
	s_branch .Lhc_dd_A1
.Lhc_d2_A1:
	s_sub_i32 s17, s14, 0xd40
	s_load_dwordx2 s[4:5], s[24:25], 0xc0
	s_add_u32 s6, s26, 0x7a00000
	s_addc_u32 s7, s27, 0
	s_movk_i32 s8, 0x800
	s_movk_i32 s9, 0x2c00
	s_lshr_b32 s10, s17, 3
	s_lshl_b32 s10, s10, 6
	s_and_b32 s11, s17, 7
	s_lshl_b32 s11, s11, 8
	s_mov_b32 s12, s11
	s_movk_i32 s13, 0x80
	s_waitcnt lgkmcnt(0)
.Lhc_dd_A1:
	s_lshl_b32 s17, s28, 3
	s_add_i32 s17, s17, s10
	s_mul_i32 s18, s17, s8
	s_add_i32 s18, s18, s11
	s_lshl_b32 s18, s18, 2
	s_add_u32 s4, s4, s18
	s_addc_u32 s5, s5, 0
	s_lshl_b32 s19, s8, 2
	global_load_dwordx4 v[2:5], v72, s[4:5] nt
	s_add_u32 s4, s4, s19
	s_addc_u32 s5, s5, 0
	global_load_dwordx4 v[6:9], v72, s[4:5] nt
	s_add_u32 s4, s4, s19
	s_addc_u32 s5, s5, 0
	global_load_dwordx4 v[10:13], v72, s[4:5] nt
	s_add_u32 s4, s4, s19
	s_addc_u32 s5, s5, 0
	global_load_dwordx4 v[14:17], v72, s[4:5] nt
	s_add_u32 s4, s4, s19
	s_addc_u32 s5, s5, 0
	global_load_dwordx4 v[18:21], v72, s[4:5] nt
	s_add_u32 s4, s4, s19
	s_addc_u32 s5, s5, 0
	global_load_dwordx4 v[22:25], v72, s[4:5] nt
	s_add_u32 s4, s4, s19
	s_addc_u32 s5, s5, 0
	global_load_dwordx4 v[26:29], v72, s[4:5] nt
	s_add_u32 s4, s4, s19
	s_addc_u32 s5, s5, 0
	global_load_dwordx4 v[30:33], v72, s[4:5] nt
	v_mul_lo_u32 v71, v68, s9
	v_lshl_add_u32 v71, v67, 4, v71
	s_lshl_b32 s17, s10, 1
	s_add_u32 s6, s6, s17
	s_addc_u32 s7, s7, 0
.Lhc_loop:
	s_add_i32 s36, s14, 1
	s_cmpk_lt_u32 s36, 0x7c0
	s_cbranch_scc0 .Lhc_d1_B2
	s_sub_i32 s17, s36, 0x5c0
	s_lshr_b32 s18, s17, 8
	s_and_b32 s17, s17, 255
	s_load_dwordx2 s[4:5], s[24:25], 0x48
	s_lshl_b32 s19, s18, 24
	s_lshl_b32 s20, s18, 23
	s_add_u32 s30, s26, 0x3e00000
	s_addc_u32 s31, s27, 0
	s_add_u32 s30, s30, s20
	s_addc_u32 s31, s31, 0
	s_movk_i32 s8, 0x800
	s_movk_i32 s32, 0x1000
	s_lshr_b32 s10, s17, 3
	s_lshl_b32 s10, s10, 6
	s_and_b32 s11, s17, 7
	s_lshl_b32 s11, s11, 8
	s_mov_b32 s33, s11
	s_movk_i32 s34, 0x80
	s_waitcnt lgkmcnt(0)
	s_add_u32 s4, s4, s19
	s_addc_u32 s5, s5, 0
	s_branch .Lhc_dd_B2
; __device__ __forceinline__ unsigned cvt_pk_bf16(float lo, float hi) { unsigned r; asm volatile("v_cvt_pk_bf16_f32 %0, %1, %2" : "=v"(r) : "v"(lo), "v"(hi)); return r; }
; #define GAS __attribute__((address_space(1)))
; #define LAS __attribute__((address_space(3)))
; template <class RowMap>
; __device__ __forceinline__ void conv_store_bf16(const f32x4 (&r)[8], unsigned char* WT, int Kbytes, int k0bytes, int n0, const RowMap rm, LAS unsigned char* T, int tid, int wave, int lane) {
;     const int c = tid & 7, rr = tid >> 3;
; #pragma unroll
;     for (int p = 0; p < 2; ++p) {
;         if ((lane >> 5) == p) {
; #pragma unroll
;             for (int j = 0; j < 4; ++j) { v4u o; o.x = pg8::cvt_pk_bf16(r[0][j], r[1][j]); o.y = pg8::cvt_pk_bf16(r[2][j], r[3][j]); o.z = pg8::cvt_pk_bf16(r[4][j], r[5][j]); o.w = pg8::cvt_pk_bf16(r[6][j], r[7][j]);
;                 *(LAS v4u*)(T + (4 * (lane & 31) + j) * 128 + 16 * (wave ^ (lane & 7))) = o; } }
;         LDS_BARRIER();
; #pragma unroll
;         for (int q = 0; q < 2; ++q) { const int row = rr + 64 * q; const v4u v = *(const LAS v4u*)(T + row * 128 + 16 * (c ^ ((row >> 2) & 7)));
;             const int dr = rm(n0 + 128 * p + row); if (dr >= 0) *(GAS v4u*)(WT + (size_t)dr * Kbytes + k0bytes + 16 * c) = v; }
;         LDS_BARRIER();
;     }
; __device__ __forceinline__ bool conv_decode(KA A, int t, ConvTile& c) {
;     ...
;     if (t < 1472) { const int l = t / 736, r = t % 736; c.W = A->in[I_WIN] + (size_t)l * D * PSRC; c.WT = ws + WS_WIN + (size_t)l * NP * D * 2; c.K = D; c.N = PSRC; c.k0 = 64 * (r / 23); c.n0 = 256 * (r % 23); c.kind = 1; return true; } t -= 1472;
;     if (t < 512) { const int l = t >> 8, r = t & 255; c.W = A->in[I_WOUT] + (size_t)l * D * D; c.WT = ws + WS_WOUT + (size_t)l * D * D * 2; c.K = D; c.N = D; c.k0 = 64 * (r >> 3); c.n0 = 256 * (r & 7); c.kind = 0; return true; } t -= 512;
;     if (t < 1408) { const int hf = t / 704, r = t % 704; c.W = hf ? A->in[I_FWU] : A->in[I_FWG]; c.WT = ws + WS_FUP; c.K = D; c.N = FF; c.k0 = 64 * (r / 22); c.n0 = 256 * (r % 22); c.kind = 2 + hf; return true; } t -= 1408;
;     if (t < 704) { c.W = A->in[I_FWD]; c.WT = ws + WS_FDN; c.K = FF; c.N = D; c.k0 = 64 * (t >> 3); c.n0 = 256 * (t & 7); c.kind = 0; return true; } t -= 704;
.Lhc_d1_B2:
	s_cmpk_lt_u32 s36, 0xd40
	s_cbranch_scc0 .Lhc_d2_B2
	s_sub_i32 s17, s36, 0x7c0
	s_cmpk_ge_u32 s17, 0x2c0
	s_cselect_b32 s18, 1, 0
	s_mul_i32 s19, s18, 0x2c0
	s_sub_i32 s17, s17, s19
	s_lshl_b32 s19, s18, 3
	s_add_u32 s20, s24, s19
	s_addc_u32 s21, s25, 0
	s_load_dwordx2 s[4:5], s[20:21], 0xb0
	s_add_u32 s30, s26, 0x4e00000
	s_addc_u32 s31, s27, 0
	s_movk_i32 s8, 0x1600
	s_movk_i32 s32, 0x1000
	s_mul_i32 s19, s17, 0xba3
	s_lshr_b32 s19, s19, 16
	s_lshl_b32 s10, s19, 6
	s_mul_i32 s19, s19, 22
	s_sub_i32 s19, s17, s19
	s_lshl_b32 s11, s19, 8
	s_lshl_b32 s33, s11, 1
	s_lshl_b32 s19, s18, 7
	s_add_i32 s33, s33, s19
	s_movk_i32 s34, 0x100
	s_waitcnt lgkmcnt(0)
	s_branch .Lhc_dd_B2
.Lhc_d2_B2:
	s_sub_i32 s17, s36, 0xd40
	s_load_dwordx2 s[4:5], s[24:25], 0xc0
	s_add_u32 s30, s26, 0x7a00000
	s_addc_u32 s31, s27, 0
	s_movk_i32 s8, 0x800
	s_movk_i32 s32, 0x2c00
	s_lshr_b32 s10, s17, 3
	s_lshl_b32 s10, s10, 6
	s_and_b32 s11, s17, 7
	s_lshl_b32 s11, s11, 8
	s_mov_b32 s33, s11
	s_movk_i32 s34, 0x80
	s_waitcnt lgkmcnt(0)
.Lhc_dd_B2:
	s_lshl_b32 s17, s28, 3
	s_add_i32 s17, s17, s10
	s_mul_i32 s18, s17, s8
	s_add_i32 s18, s18, s11
	s_lshl_b32 s18, s18, 2
	s_add_u32 s4, s4, s18
	s_addc_u32 s5, s5, 0
	s_lshl_b32 s19, s8, 2
	global_load_dwordx4 v[74:77], v72, s[4:5] nt
	s_add_u32 s4, s4, s19
	s_addc_u32 s5, s5, 0
	global_load_dwordx4 v[78:81], v72, s[4:5] nt
	s_add_u32 s4, s4, s19
	s_addc_u32 s5, s5, 0
	global_load_dwordx4 v[82:85], v72, s[4:5] nt
	s_add_u32 s4, s4, s19
	s_addc_u32 s5, s5, 0
	global_load_dwordx4 v[86:89], v72, s[4:5] nt
	s_add_u32 s4, s4, s19
	s_addc_u32 s5, s5, 0
	global_load_dwordx4 v[90:93], v72, s[4:5] nt
	s_add_u32 s4, s4, s19
	s_addc_u32 s5, s5, 0
	global_load_dwordx4 v[94:97], v72, s[4:5] nt
	s_add_u32 s4, s4, s19
	s_addc_u32 s5, s5, 0
	global_load_dwordx4 v[98:101], v72, s[4:5] nt
	s_add_u32 s4, s4, s19
	s_addc_u32 s5, s5, 0
	global_load_dwordx4 v[102:105], v72, s[4:5] nt
	v_mul_lo_u32 v73, v68, s32
	v_lshl_add_u32 v73, v67, 4, v73
	s_lshl_b32 s17, s10, 1
	s_add_u32 s30, s30, s17
	s_addc_u32 s31, s31, 0
	s_waitcnt vmcnt(8)
	v_cvt_pk_bf16_f32 v34, v2, v6
	v_cvt_pk_bf16_f32 v35, v10, v14
	v_cvt_pk_bf16_f32 v36, v18, v22
	v_cvt_pk_bf16_f32 v37, v26, v30
	v_cvt_pk_bf16_f32 v38, v3, v7
	v_cvt_pk_bf16_f32 v39, v11, v15
	v_cvt_pk_bf16_f32 v40, v19, v23
	v_cvt_pk_bf16_f32 v41, v27, v31
	v_cvt_pk_bf16_f32 v42, v4, v8
	v_cvt_pk_bf16_f32 v43, v12, v16
	v_cvt_pk_bf16_f32 v44, v20, v24
	v_cvt_pk_bf16_f32 v45, v28, v32
	v_cvt_pk_bf16_f32 v46, v5, v9
	v_cvt_pk_bf16_f32 v47, v13, v17
	v_cvt_pk_bf16_f32 v48, v21, v25
	v_cvt_pk_bf16_f32 v49, v29, v33
	s_mov_b32 exec_lo, -1
	s_mov_b32 exec_hi, 0
	ds_write_b128 v69, v[34:37]
	ds_write_b128 v69, v[38:41] offset:128
	ds_write_b128 v69, v[42:45] offset:256
	ds_write_b128 v69, v[46:49] offset:384
	s_mov_b64 exec, -1
	s_waitcnt lgkmcnt(0)
	s_barrier
	ds_read_b128 v[50:53], v70
	ds_read_b128 v[54:57], v70 offset:8192
	s_mov_b32 s17, s12
	s_mul_i32 s20, s17, s9
	s_add_u32 s20, s6, s20
	s_addc_u32 s21, s7, 0
	s_lshl_b32 s22, s9, 6
	s_add_u32 s22, s20, s22
	s_addc_u32 s23, s21, 0
	s_waitcnt lgkmcnt(1)
	global_store_dwordx4 v71, v[50:53], s[20:21]
	s_waitcnt lgkmcnt(0)
	global_store_dwordx4 v71, v[54:57], s[22:23]
	s_barrier
	s_mov_b32 exec_lo, 0
	s_mov_b32 exec_hi, -1
	ds_write_b128 v69, v[34:37]
	ds_write_b128 v69, v[38:41] offset:128
	ds_write_b128 v69, v[42:45] offset:256
	ds_write_b128 v69, v[46:49] offset:384
	s_mov_b64 exec, -1
	s_waitcnt lgkmcnt(0)
	s_barrier
	ds_read_b128 v[50:53], v70
	ds_read_b128 v[54:57], v70 offset:8192
	s_add_i32 s17, s12, s13
	s_mul_i32 s20, s17, s9
	s_add_u32 s20, s6, s20
	s_addc_u32 s21, s7, 0
	s_lshl_b32 s22, s9, 6
	s_add_u32 s22, s20, s22
	s_addc_u32 s23, s21, 0
	s_waitcnt lgkmcnt(1)
	global_store_dwordx4 v71, v[50:53], s[20:21]
	s_waitcnt lgkmcnt(0)
	global_store_dwordx4 v71, v[54:57], s[22:23]
	s_barrier
	s_addk_i32 s15, 0x100
	s_cmpk_lt_u32 s15, 0x800
	s_cselect_b32 s35, 1, 0
	s_cbranch_scc0 .Lhc_nonext
	s_lshl_b32 s14, s15, 1
	s_cmpk_lt_u32 s14, 0x7c0
	s_cbranch_scc0 .Lhc_d1_A3
	s_sub_i32 s17, s14, 0x5c0
	s_lshr_b32 s18, s17, 8
	s_and_b32 s17, s17, 255
	s_load_dwordx2 s[4:5], s[24:25], 0x48
	s_lshl_b32 s19, s18, 24
	s_lshl_b32 s20, s18, 23
	s_add_u32 s6, s26, 0x3e00000
	s_addc_u32 s7, s27, 0
	s_add_u32 s6, s6, s20
	s_addc_u32 s7, s7, 0
	s_movk_i32 s8, 0x800
	s_movk_i32 s9, 0x1000
	s_lshr_b32 s10, s17, 3
	s_lshl_b32 s10, s10, 6
	s_and_b32 s11, s17, 7
	s_lshl_b32 s11, s11, 8
	s_mov_b32 s12, s11
	s_movk_i32 s13, 0x80
	s_waitcnt lgkmcnt(0)
	s_add_u32 s4, s4, s19
	s_addc_u32 s5, s5, 0
	s_branch .Lhc_dd_A3

; __device__ __forceinline__ unsigned cvt_pk_bf16(float lo, float hi) { unsigned r; asm volatile("v_cvt_pk_bf16_f32 %0, %1, %2" : "=v"(r) : "v"(lo), "v"(hi)); return r; }
; #define GAS __attribute__((address_space(1)))
; #define LAS __attribute__((address_space(3)))
; #define LDS_BARRIER() do { asm volatile("s_waitcnt lgkmcnt(0)" ::: "memory"); __builtin_amdgcn_s_barrier(); asm volatile("" ::: "memory"); } while (0)
; __device__ __forceinline__ void conv_load(const float* W, int N, int k0, int n0, int wave, int lane, f32x4 (&r)[8]) {
;     const int n = n0 + 4 * lane; const bool ok = n < N;
;     const float* p = W + (size_t)(k0 + 8 * wave) * N + n;
; #pragma unroll
;     for (int i = 0; i < 8; ++i) r[i] = ok ? __builtin_nontemporal_load((const GAS f32x4*)(p + (size_t)i * N)) : (f32x4){0.f, 0.f, 0.f, 0.f};
; }
; template <class RowMap>
; __device__ __forceinline__ void conv_store_bf16(const f32x4 (&r)[8], unsigned char* WT, int Kbytes, int k0bytes, int n0, const RowMap rm, LAS unsigned char* T, int tid, int wave, int lane) {
;     const int c = tid & 7, rr = tid >> 3;
; #pragma unroll
;     for (int p = 0; p < 2; ++p) {
;         if ((lane >> 5) == p) {
; #pragma unroll
;             for (int j = 0; j < 4; ++j) { v4u o; o.x = pg8::cvt_pk_bf16(r[0][j], r[1][j]); o.y = pg8::cvt_pk_bf16(r[2][j], r[3][j]); o.z = pg8::cvt_pk_bf16(r[4][j], r[5][j]); o.w = pg8::cvt_pk_bf16(r[6][j], r[7][j]);
;                 *(LAS v4u*)(T + (4 * (lane & 31) + j) * 128 + 16 * (wave ^ (lane & 7))) = o; } }
;         LDS_BARRIER();
; #pragma unroll
;         for (int q = 0; q < 2; ++q) { const int row = rr + 64 * q; const v4u v = *(const LAS v4u*)(T + row * 128 + 16 * (c ^ ((row >> 2) & 7)));
;             const int dr = rm(n0 + 128 * p + row); if (dr >= 0) *(GAS v4u*)(WT + (size_t)dr * Kbytes + k0bytes + 16 * c) = v; }
;         LDS_BARRIER();
;     }
.Lhc_dd_A3:
	s_lshl_b32 s17, s28, 3
	s_add_i32 s17, s17, s10
	s_mul_i32 s18, s17, s8
	s_add_i32 s18, s18, s11
	s_lshl_b32 s18, s18, 2
	s_add_u32 s4, s4, s18
	s_addc_u32 s5, s5, 0
	s_lshl_b32 s19, s8, 2
	global_load_dwordx4 v[2:5], v72, s[4:5] nt
	s_add_u32 s4, s4, s19
	s_addc_u32 s5, s5, 0
	global_load_dwordx4 v[6:9], v72, s[4:5] nt
	s_add_u32 s4, s4, s19
	s_addc_u32 s5, s5, 0
	global_load_dwordx4 v[10:13], v72, s[4:5] nt
	s_add_u32 s4, s4, s19
	s_addc_u32 s5, s5, 0
	global_load_dwordx4 v[14:17], v72, s[4:5] nt
	s_add_u32 s4, s4, s19
	s_addc_u32 s5, s5, 0
	global_load_dwordx4 v[18:21], v72, s[4:5] nt
	s_add_u32 s4, s4, s19
	s_addc_u32 s5, s5, 0
	global_load_dwordx4 v[22:25], v72, s[4:5] nt
	s_add_u32 s4, s4, s19
	s_addc_u32 s5, s5, 0
	global_load_dwordx4 v[26:29], v72, s[4:5] nt
	s_add_u32 s4, s4, s19
	s_addc_u32 s5, s5, 0
	global_load_dwordx4 v[30:33], v72, s[4:5] nt
	v_mul_lo_u32 v71, v68, s9
	v_lshl_add_u32 v71, v67, 4, v71
	s_lshl_b32 s17, s10, 1
	s_add_u32 s6, s6, s17
	s_addc_u32 s7, s7, 0
	s_waitcnt vmcnt(12)
	s_branch .Lhc_pb
.Lhc_nonext:
	s_waitcnt vmcnt(4)
.Lhc_pb:
	v_cvt_pk_bf16_f32 v34, v74, v78
	v_cvt_pk_bf16_f32 v35, v82, v86
	v_cvt_pk_bf16_f32 v36, v90, v94
	v_cvt_pk_bf16_f32 v37, v98, v102
	v_cvt_pk_bf16_f32 v38, v75, v79
	v_cvt_pk_bf16_f32 v39, v83, v87
	v_cvt_pk_bf16_f32 v40, v91, v95
	v_cvt_pk_bf16_f32 v41, v99, v103
	v_cvt_pk_bf16_f32 v42, v76, v80
	v_cvt_pk_bf16_f32 v43, v84, v88
	v_cvt_pk_bf16_f32 v44, v92, v96
	v_cvt_pk_bf16_f32 v45, v100, v104
	v_cvt_pk_bf16_f32 v46, v77, v81
	v_cvt_pk_bf16_f32 v47, v85, v89
	v_cvt_pk_bf16_f32 v48, v93, v97
	v_cvt_pk_bf16_f32 v49, v101, v105
	s_mov_b32 exec_lo, -1
	s_mov_b32 exec_hi, 0
	ds_write_b128 v69, v[34:37]
	ds_write_b128 v69, v[38:41] offset:128
	ds_write_b128 v69, v[42:45] offset:256
	ds_write_b128 v69, v[46:49] offset:384
	s_mov_b64 exec, -1
	s_waitcnt lgkmcnt(0)
	s_barrier
	ds_read_b128 v[50:53], v70
	ds_read_b128 v[54:57], v70 offset:8192
	s_mov_b32 s17, s33
	s_mul_i32 s20, s17, s32
	s_add_u32 s20, s30, s20
	s_addc_u32 s21, s31, 0
	s_lshl_b32 s22, s32, 6
	s_add_u32 s22, s20, s22
	s_addc_u32 s23, s21, 0
	s_waitcnt lgkmcnt(1)
	global_store_dwordx4 v73, v[50:53], s[20:21]
	s_waitcnt lgkmcnt(0)
	global_store_dwordx4 v73, v[54:57], s[22:23]
	s_barrier
	s_mov_b32 exec_lo, 0
	s_mov_b32 exec_hi, -1
	ds_write_b128 v69, v[34:37]
	ds_write_b128 v69, v[38:41] offset:128
	ds_write_b128 v69, v[42:45] offset:256
	ds_write_b128 v69, v[46:49] offset:384
	s_mov_b64 exec, -1
	s_waitcnt lgkmcnt(0)
	s_barrier
	ds_read_b128 v[50:53], v70
	ds_read_b128 v[54:57], v70 offset:8192
	s_add_i32 s17, s33, s34
	s_mul_i32 s20, s17, s32
	s_add_u32 s20, s30, s20
	s_addc_u32 s21, s31, 0
	s_lshl_b32 s22, s32, 6
	s_add_u32 s22, s20, s22
	s_addc_u32 s23, s21, 0
	s_waitcnt lgkmcnt(1)
	global_store_dwordx4 v73, v[50:53], s[20:21]
	s_waitcnt lgkmcnt(0)
	global_store_dwordx4 v73, v[54:57], s[22:23]
	s_barrier
	s_cmp_lg_u32 s35, 0
	s_cbranch_scc1 .Lhc_loop
	v_readlane_b32 s4, v255, 25
	v_readlane_b32 s5, v255, 26
	v_readlane_b32 s6, v255, 27
	v_readlane_b32 s7, v255, 28
	v_readlane_b32 s8, v255, 29
	v_readlane_b32 s9, v255, 30
	v_readlane_b32 s10, v255, 31
	v_readlane_b32 s11, v255, 32
	v_readlane_b32 s12, v255, 33
	v_readlane_b32 s13, v255, 34
	v_readlane_b32 s14, v255, 35
	v_readlane_b32 s15, v255, 36
	v_readlane_b32 s16, v255, 37
	v_readlane_b32 s17, v255, 38
	v_readlane_b32 s18, v255, 39
	v_readlane_b32 s19, v255, 40
	v_readlane_b32 s20, v255, 41
	v_readlane_b32 s21, v255, 42
	v_readlane_b32 s22, v255, 43
	v_readlane_b32 s23, v255, 44
	v_readlane_b32 s24, v255, 45
	v_readlane_b32 s25, v255, 46
	v_readlane_b32 s26, v255, 47
	v_readlane_b32 s27, v255, 48
	v_readlane_b32 s28, v255, 49
	v_readlane_b32 s29, v255, 50
	v_readlane_b32 s30, v255, 51
	v_readlane_b32 s31, v255, 52
	v_readlane_b32 s32, v255, 53
	v_readlane_b32 s33, v255, 54
	v_readlane_b32 s34, v255, 55
	v_readlane_b32 s35, v255, 56
	v_readlane_b32 s36, v255, 57
	v_readlane_b32 s37, v255, 58
	v_readlane_b32 s38, v255, 59
	v_readlane_b32 s39, v255, 60
	s_nop 3
.Lhc_skip:
	v_readlane_b32 s4, v254, 38
	v_readlane_b32 s5, v254, 39
	v_readlane_b32 s6, v255, 18
	v_readlane_b32 s12, v254, 36
	s_movk_i32 s2, 0x1c00
	s_andn2_b64 vcc, exec, s[4:5]
	v_readlane_b32 s10, v254, 48
	v_readlane_b32 s11, v254, 49
	v_readlane_b32 s4, v254, 46
	v_readlane_b32 s7, v255, 19
	v_readlane_b32 s13, v254, 37
	v_readlane_b32 s5, v254, 47
	s_cbranch_vccnz .LBB0_766
	v_readlane_b32 s4, v254, 40
	v_readlane_b32 s5, v254, 41
	s_mov_b64 s[12:13], -1
	s_and_b64 vcc, exec, s[4:5]
	s_cbranch_vccz .LBB0_765
	s_lshl_b32 s1, s0, 3
	s_mov_b64 s[12:13], 0
